# final phase: final gain vector loaded once before the row loop; output stage has no loads and no vmcnt(0) waits
# speedup vs baseline: 1.0223x; 1.0138x over previous
.LBB0_2446:
	s_or_b64 exec, exec, s[4:5]
	s_waitcnt lgkmcnt(0)
	v_mov_b32_e32 v0, s2
	s_barrier
	v_mbcnt_lo_u32_b32 v4, -1, 0
	v_mbcnt_hi_u32_b32 v4, -1, v4
	s_mov_b32 s8, 0
	v_readfirstlane_b32 s16, v0
	v_mov_b32_e32 v0, 0
	s_load_dwordx4 s[4:7], s[48:49], 0x178
	s_load_dwordx2 s[0:1], s[48:49], 0x188
	v_readfirstlane_b32 s2, v0
	s_ashr_i32 s3, s2, 31
	v_ashrrev_i32_e32 v5, 31, v4
	v_lshlrev_b64 v[0:1], 4, v[4:5]
	s_waitcnt lgkmcnt(0)
	s_add_u32 s2, s0, s2
	s_addc_u32 s3, s1, s3
	v_lshl_add_u64 v[2:3], s[2:3], 0, v[0:1]
	s_mov_b64 s[0:1], 0x2bc80000
	s_add_u32 s9, s2, 0x460000
	v_lshl_add_u64 v[6:7], v[2:3], 0, s[0:1]
	v_lshl_add_u64 v[2:3], v[4:5], 3, s[2:3]
	s_mov_b64 s[0:1], 0x48a80000
	s_addc_u32 s10, s3, 0
	v_lshl_add_u64 v[8:9], v[2:3], 0, s[0:1]
	v_lshl_add_u64 v[10:11], s[4:5], 0, v[0:1]
	s_mov_b64 s[0:1], 0x1000
	s_add_u32 s11, s2, 0x470000
	v_lshl_add_u64 v[12:13], v[10:11], 0, s[0:1]
	s_mov_b64 s[0:1], 0x1400
	s_addc_u32 s12, s3, 0
	v_lshl_add_u64 v[14:15], v[10:11], 0, s[0:1]
	s_mov_b64 s[0:1], 0x1800
	s_add_u32 s13, s2, 0x480000
	v_lshl_add_u64 v[16:17], v[10:11], 0, s[0:1]
	s_mov_b64 s[0:1], 0x1c00
	s_addc_u32 s14, s3, 0
	s_lshl_b32 s15, s16, 5
	v_lshlrev_b32_e32 v2, 2, v4
	v_lshl_add_u64 v[18:19], v[10:11], 0, s[0:1]
	s_lshl_b32 s0, s16, 6
	v_readlane_b32 s1, v254, 22
	v_mov_b32_e32 v24, 0
	s_add_i32 s15, s15, s76
	v_xor_b32_e32 v25, 64, v2
	v_xor_b32_e32 v26, 0x80, v2
	v_lshl_add_u64 v[20:21], s[6:7], 0, v[0:1]
	s_add_i32 s4, s0, s1
	s_add_i32 s16, 0, 0x27c40
	s_mov_b64 s[6:7], 0x40a000
	s_movk_i32 s17, 0x1000
	s_mov_b32 s18, 0x40b000
	v_mov_b32_e32 v27, 0x358637bd
	s_mov_b32 s19, 0xf800000
	v_mov_b32_e32 v28, 0x260
	global_load_dwordx4 v[176:179], v[10:11], off
	global_load_dwordx4 v[180:183], v[10:11], off offset:1024
	global_load_dwordx4 v[184:187], v[10:11], off offset:2048
	global_load_dwordx4 v[188:191], v[10:11], off offset:3072
	global_load_dwordx4 v[192:195], v[12:13], off
	global_load_dwordx4 v[196:199], v[14:15], off
	global_load_dwordx4 v[200:203], v[16:17], off
	global_load_dwordx4 v[204:207], v[18:19], off
.LBB0_2447:
	s_add_i32 s0, s15, s8
	s_ashr_i32 s1, s0, 31
	s_lshr_b32 s5, s1, 21
	s_add_i32 s5, s0, s5
	s_ashr_i32 s5, s5, 11
	s_add_i32 s5, s5, 4
	s_mul_hi_i32 s21, s5, 0xc000
	s_mul_i32 s5, s5, 0xc000
	s_add_u32 s20, s2, s5
	s_addc_u32 s21, s3, s21
	s_ashr_i32 s5, s4, 31
	s_lshl_b64 s[22:23], s[4:5], 2
	v_lshl_add_u64 v[22:23], v[4:5], 4, s[20:21]
	s_add_u32 s20, s9, s22
	v_lshl_add_u64 v[62:63], v[22:23], 0, s[6:7]
	v_add_co_u32_e32 v22, vcc, s18, v22
	s_nop 0
	v_addc_co_u32_e32 v23, vcc, 0, v23, vcc
	s_addc_u32 s21, s10, s23
	global_load_dwordx4 v[30:33], v[62:63], off offset:1024
	global_load_dwordx4 v[34:37], v[62:63], off offset:2048
	global_load_dwordx4 v[38:41], v[62:63], off offset:3072
	global_load_dwordx4 v[42:45], v[22:23], off offset:-4096
	global_load_dwordx4 v[46:49], v[22:23], off
	global_load_dwordx4 v[50:53], v[22:23], off offset:1024
	global_load_dwordx4 v[54:57], v[22:23], off offset:2048
	global_load_dwordx4 v[58:61], v[22:23], off offset:3072
	global_load_dwordx2 v[94:95], v24, s[20:21]
	s_add_u32 s20, s11, s22
	s_addc_u32 s21, s12, s23
	s_add_i32 s24, s4, 1
	s_ashr_i32 s25, s24, 31
	global_load_dword v29, v24, s[20:21]
	s_lshl_b64 s[20:21], s[24:25], 2
	s_add_u32 s24, s11, s20
	s_addc_u32 s25, s12, s21
	global_load_dword v97, v24, s[24:25]
	s_add_u32 s22, s13, s22
	s_addc_u32 s23, s14, s23
	s_add_u32 s20, s13, s20
	s_addc_u32 s21, s14, s21
	s_lshl_b64 s[0:1], s[0:1], 13
	v_lshl_add_u64 v[78:79], v[6:7], 0, s[0:1]
	v_add_co_u32_e32 v100, vcc, s17, v78
	global_load_dword v96, v24, s[22:23]
	global_load_dword v98, v24, s[20:21]
	v_addc_co_u32_e32 v101, vcc, 0, v79, vcc
	global_load_dwordx4 v[62:65], v[78:79], off
	global_load_dwordx4 v[66:69], v[78:79], off offset:1024
	global_load_dwordx4 v[70:73], v[78:79], off offset:2048
	global_load_dwordx4 v[74:77], v[78:79], off offset:3072
	s_nop 0
	global_load_dwordx4 v[78:81], v[100:101], off
	global_load_dwordx4 v[82:85], v[100:101], off offset:1024
	global_load_dwordx4 v[86:89], v[100:101], off offset:2048
	global_load_dwordx4 v[90:93], v[100:101], off offset:3072
	v_lshl_add_u64 v[22:23], v[20:21], 0, s[0:1]
	s_add_i32 s8, s8, 8
	s_add_i32 s4, s4, 16
	s_cmp_lg_u32 s8, 32
	s_waitcnt vmcnt(12)
	v_lshlrev_b32_e32 v94, 2, v94
	v_lshlrev_b32_e32 v95, 2, v95
	v_add_u32_e32 v94, s16, v94
	v_add_u32_e32 v95, s16, v95
	ds_read_b32 v94, v94
	ds_read_b32 v95, v95
	s_waitcnt lgkmcnt(1)
	v_lshlrev_b32_e32 v94, 8, v94
	s_waitcnt lgkmcnt(0)
	v_lshlrev_b32_e32 v95, 8, v95
	s_waitcnt vmcnt(11)
	v_add_u32_e32 v94, v94, v29
	s_waitcnt vmcnt(10)
	v_add_u32_e32 v100, v95, v97
	v_ashrrev_i32_e32 v95, 31, v94
	v_ashrrev_i32_e32 v101, 31, v100
	v_lshlrev_b64 v[94:95], 12, v[94:95]
	v_lshlrev_b64 v[100:101], 12, v[100:101]
	v_lshl_add_u64 v[94:95], v[8:9], 0, v[94:95]
	v_lshl_add_u64 v[100:101], v[8:9], 0, v[100:101]
	global_load_dwordx2 v[102:103], v[94:95], off
	global_load_dwordx2 v[104:105], v[100:101], off
	global_load_dwordx2 v[106:107], v[94:95], off offset:512
	global_load_dwordx2 v[108:109], v[100:101], off offset:512
	global_load_dwordx2 v[110:111], v[94:95], off offset:1024
	global_load_dwordx2 v[112:113], v[100:101], off offset:1024
	global_load_dwordx2 v[114:115], v[94:95], off offset:1536
	global_load_dwordx2 v[116:117], v[100:101], off offset:1536
	global_load_dwordx2 v[118:119], v[94:95], off offset:2048
	global_load_dwordx2 v[120:121], v[100:101], off offset:2048
	global_load_dwordx2 v[122:123], v[94:95], off offset:2560
	global_load_dwordx2 v[124:125], v[100:101], off offset:2560
	global_load_dwordx2 v[126:127], v[94:95], off offset:3072
	global_load_dwordx2 v[128:129], v[100:101], off offset:3072
	s_nop 0
	global_load_dwordx2 v[94:95], v[94:95], off offset:3584
	s_nop 0
	global_load_dwordx2 v[100:101], v[100:101], off offset:3584
	s_waitcnt vmcnt(15)
	v_lshlrev_b32_e32 v130, 16, v102
	s_waitcnt vmcnt(14)
	v_lshlrev_b32_e32 v132, 16, v104
	v_and_b32_e32 v133, 0xffff0000, v104
	v_lshlrev_b32_e32 v104, 16, v105
	v_and_b32_e32 v105, 0xffff0000, v105
	s_waitcnt vmcnt(12)
	v_lshlrev_b32_e32 v136, 16, v108
	v_and_b32_e32 v137, 0xffff0000, v108
	v_lshlrev_b32_e32 v108, 16, v109
	v_and_b32_e32 v109, 0xffff0000, v109
	v_and_b32_e32 v131, 0xffff0000, v102
	v_lshlrev_b32_e32 v102, 16, v103
	v_and_b32_e32 v103, 0xffff0000, v103
	v_lshlrev_b32_e32 v134, 16, v106
	v_and_b32_e32 v135, 0xffff0000, v106
	v_lshlrev_b32_e32 v106, 16, v107
	v_and_b32_e32 v107, 0xffff0000, v107
	s_waitcnt vmcnt(10)
	v_lshlrev_b32_e32 v140, 16, v112
	v_and_b32_e32 v141, 0xffff0000, v112
	v_lshlrev_b32_e32 v112, 16, v113
	v_and_b32_e32 v113, 0xffff0000, v113
	v_pk_mul_f32 v[104:105], v[98:99], v[104:105] op_sel_hi:[0,1]
	v_pk_mul_f32 v[132:133], v[98:99], v[132:133] op_sel_hi:[0,1]
	v_pk_mul_f32 v[108:109], v[98:99], v[108:109] op_sel_hi:[0,1]
	v_pk_mul_f32 v[136:137], v[98:99], v[136:137] op_sel_hi:[0,1]
	v_lshlrev_b32_e32 v138, 16, v110
	v_and_b32_e32 v139, 0xffff0000, v110
	v_lshlrev_b32_e32 v110, 16, v111
	v_and_b32_e32 v111, 0xffff0000, v111
	v_pk_mul_f32 v[140:141], v[98:99], v[140:141] op_sel_hi:[0,1]
	v_pk_mul_f32 v[112:113], v[98:99], v[112:113] op_sel_hi:[0,1]
	v_pk_fma_f32 v[130:131], v[96:97], v[130:131], v[132:133] op_sel_hi:[0,1,1]
	v_pk_fma_f32 v[102:103], v[96:97], v[102:103], v[104:105] op_sel_hi:[0,1,1]
	v_pk_fma_f32 v[104:105], v[96:97], v[134:135], v[136:137] op_sel_hi:[0,1,1]
	v_pk_fma_f32 v[106:107], v[96:97], v[106:107], v[108:109] op_sel_hi:[0,1,1]
	s_waitcnt vmcnt(8)
	v_lshlrev_b32_e32 v144, 16, v116
	v_and_b32_e32 v145, 0xffff0000, v116
	v_lshlrev_b32_e32 v116, 16, v117
	v_and_b32_e32 v117, 0xffff0000, v117
	s_waitcnt vmcnt(4)
	v_lshlrev_b32_e32 v152, 16, v124
	v_and_b32_e32 v153, 0xffff0000, v124
	v_lshlrev_b32_e32 v124, 16, v125
	v_and_b32_e32 v125, 0xffff0000, v125
	s_waitcnt vmcnt(2)
	v_lshlrev_b32_e32 v156, 16, v128
	v_and_b32_e32 v157, 0xffff0000, v128
	v_pk_fma_f32 v[108:109], v[96:97], v[110:111], v[112:113] op_sel_hi:[0,1,1]
	v_pk_fma_f32 v[110:111], v[96:97], v[138:139], v[140:141] op_sel_hi:[0,1,1]
	v_pk_fma_f32 v[44:45], v[44:45], v[102:103], v[64:65]
	v_pk_fma_f32 v[42:43], v[42:43], v[130:131], v[62:63]
	v_pk_fma_f32 v[32:33], v[32:33], v[106:107], v[68:69]
	v_pk_fma_f32 v[30:31], v[30:31], v[104:105], v[66:67]
	v_lshlrev_b32_e32 v142, 16, v114
	v_and_b32_e32 v143, 0xffff0000, v114
	v_lshlrev_b32_e32 v114, 16, v115
	v_and_b32_e32 v115, 0xffff0000, v115
	v_lshlrev_b32_e32 v148, 16, v120
	v_and_b32_e32 v149, 0xffff0000, v120
	v_lshlrev_b32_e32 v120, 16, v121
	v_and_b32_e32 v121, 0xffff0000, v121
	v_lshlrev_b32_e32 v150, 16, v122
	v_and_b32_e32 v151, 0xffff0000, v122
	v_lshlrev_b32_e32 v122, 16, v123
	v_and_b32_e32 v123, 0xffff0000, v123
	v_lshlrev_b32_e32 v154, 16, v126
	v_and_b32_e32 v155, 0xffff0000, v126
	v_pk_mul_f32 v[116:117], v[98:99], v[116:117] op_sel_hi:[0,1]
	v_pk_mul_f32 v[144:145], v[98:99], v[144:145] op_sel_hi:[0,1]
	v_pk_mul_f32 v[124:125], v[98:99], v[124:125] op_sel_hi:[0,1]
	v_pk_mul_f32 v[156:157], v[98:99], v[156:157] op_sel_hi:[0,1]
	v_pk_fma_f32 v[34:35], v[34:35], v[110:111], v[70:71]
	v_pk_fma_f32 v[36:37], v[36:37], v[108:109], v[72:73]
	v_mov_b32_e32 v64, v43
	v_mov_b32_e32 v65, v31
	v_mov_b32_e32 v68, v45
	v_mov_b32_e32 v69, v33
	v_lshlrev_b32_e32 v146, 16, v118
	v_and_b32_e32 v147, 0xffff0000, v118
	v_lshlrev_b32_e32 v118, 16, v119
	v_and_b32_e32 v119, 0xffff0000, v119
	v_lshlrev_b32_e32 v128, 16, v129
	v_and_b32_e32 v129, 0xffff0000, v129
	v_pk_mul_f32 v[120:121], v[98:99], v[120:121] op_sel_hi:[0,1]
	v_pk_mul_f32 v[148:149], v[98:99], v[148:149] op_sel_hi:[0,1]
	v_pk_fma_f32 v[112:113], v[96:97], v[142:143], v[144:145] op_sel_hi:[0,1,1]
	v_pk_fma_f32 v[114:115], v[96:97], v[114:115], v[116:117] op_sel_hi:[0,1,1]
	v_pk_fma_f32 v[122:123], v[96:97], v[122:123], v[124:125] op_sel_hi:[0,1,1]
	v_pk_fma_f32 v[124:125], v[96:97], v[154:155], v[156:157] op_sel_hi:[0,1,1]
	v_mov_b32_e32 v62, v42
	v_mov_b32_e32 v63, v30
	v_mov_b32_e32 v66, v44
	v_mov_b32_e32 v67, v32
	v_pk_mul_f32 v[70:71], v[36:37], v[36:37]
	v_pk_mul_f32 v[72:73], v[34:35], v[34:35]
	v_pk_mul_f32 v[64:65], v[64:65], v[64:65]
	v_pk_mul_f32 v[68:69], v[68:69], v[68:69]
	v_lshlrev_b32_e32 v126, 16, v127
	v_and_b32_e32 v127, 0xffff0000, v127
	v_pk_mul_f32 v[152:153], v[98:99], v[152:153] op_sel_hi:[0,1]
	v_pk_mul_f32 v[128:129], v[98:99], v[128:129] op_sel_hi:[0,1]
	v_pk_fma_f32 v[116:117], v[96:97], v[146:147], v[148:149] op_sel_hi:[0,1,1]
	v_pk_fma_f32 v[118:119], v[96:97], v[118:119], v[120:121] op_sel_hi:[0,1,1]
	v_pk_fma_f32 v[40:41], v[40:41], v[114:115], v[76:77]
	v_pk_fma_f32 v[38:39], v[38:39], v[112:113], v[74:75]
	v_pk_fma_f32 v[54:55], v[54:55], v[124:125], v[86:87]
	v_pk_mov_b32 v[86:87], v[72:73], v[70:71] op_sel:[1,0]
	v_mov_b32_e32 v73, v71
	v_pk_fma_f32 v[62:63], v[62:63], v[62:63], v[64:65]
	v_pk_fma_f32 v[64:65], v[66:67], v[66:67], v[68:69]
	v_pk_fma_f32 v[120:121], v[96:97], v[150:151], v[152:153] op_sel_hi:[0,1,1]
	v_pk_fma_f32 v[126:127], v[96:97], v[126:127], v[128:129] op_sel_hi:[0,1,1]
	v_pk_fma_f32 v[48:49], v[48:49], v[118:119], v[80:81]
	v_pk_fma_f32 v[46:47], v[46:47], v[116:117], v[78:79]
	v_mul_f32_e32 v74, v39, v39
	v_mul_f32_e32 v76, v41, v41
	v_pk_add_f32 v[66:67], v[86:87], v[72:73]
	v_pk_add_f32 v[62:63], v[62:63], v[64:65]
	s_waitcnt vmcnt(0)
	v_lshlrev_b32_e32 v160, 16, v100
	v_and_b32_e32 v161, 0xffff0000, v100
	v_lshlrev_b32_e32 v100, 16, v101
	v_and_b32_e32 v101, 0xffff0000, v101
	v_pk_fma_f32 v[52:53], v[52:53], v[122:123], v[84:85]
	v_pk_fma_f32 v[50:51], v[50:51], v[120:121], v[82:83]
	v_pk_fma_f32 v[56:57], v[56:57], v[126:127], v[88:89]
	v_mul_f32_e32 v29, v46, v46
	v_mul_f32_e32 v85, v47, v47
	v_mul_f32_e32 v88, v48, v48
	v_mul_f32_e32 v89, v49, v49
	v_pk_fma_f32 v[70:71], v[38:39], v[38:39], v[74:75] op_sel_hi:[1,1,0]
	v_pk_fma_f32 v[74:75], v[40:41], v[40:41], v[76:77] op_sel_hi:[1,1,0]
	v_pk_add_f32 v[64:65], v[66:67], v[66:67] op_sel:[0,1] op_sel_hi:[1,0]
	v_pk_add_f32 v[62:63], v[62:63], v[62:63] op_sel:[0,1] op_sel_hi:[1,0]
	v_lshlrev_b32_e32 v158, 16, v94
	v_and_b32_e32 v159, 0xffff0000, v94
	v_lshlrev_b32_e32 v94, 16, v95
	v_and_b32_e32 v95, 0xffff0000, v95
	v_pk_mul_f32 v[100:101], v[98:99], v[100:101] op_sel_hi:[0,1]
	v_pk_mul_f32 v[98:99], v[98:99], v[160:161] op_sel_hi:[0,1]
	v_pk_mul_f32 v[78:79], v[52:53], v[52:53]
	v_pk_mul_f32 v[80:81], v[50:51], v[50:51]
	v_mov_b32_e32 v71, v88
	v_mov_b32_e32 v75, v89
	v_mov_b32_e32 v65, v85
	v_mov_b32_e32 v63, v29
	v_pk_fma_f32 v[98:99], v[96:97], v[158:159], v[98:99] op_sel_hi:[0,1,1]
	v_pk_fma_f32 v[94:95], v[96:97], v[94:95], v[100:101] op_sel_hi:[0,1,1]
	v_pk_mov_b32 v[76:77], v[80:81], v[78:79] op_sel:[1,0]
	v_mov_b32_e32 v81, v79
	v_pk_add_f32 v[66:67], v[70:71], v[74:75]
	v_pk_add_f32 v[62:63], v[62:63], v[64:65]
	v_pk_fma_f32 v[60:61], v[60:61], v[94:95], v[92:93]
	v_pk_fma_f32 v[58:59], v[58:59], v[98:99], v[90:91]
	v_mul_f32_e32 v82, v55, v55
	v_mul_f32_e32 v84, v57, v57
	v_pk_add_f32 v[68:69], v[76:77], v[80:81]
	v_pk_add_f32 v[62:63], v[62:63], v[66:67]
	v_mul_f32_e32 v90, v58, v58
	v_mul_f32_e32 v91, v59, v59
	v_mul_f32_e32 v92, v60, v60
	v_mul_f32_e32 v93, v61, v61
	v_pk_fma_f32 v[78:79], v[54:55], v[54:55], v[82:83] op_sel_hi:[1,1,0]
	v_pk_fma_f32 v[82:83], v[56:57], v[56:57], v[84:85] op_sel_hi:[1,1,0]
	v_pk_add_f32 v[68:69], v[68:69], v[68:69] op_sel:[0,1] op_sel_hi:[1,0]
	v_pk_add_f32 v[62:63], v[62:63], v[62:63] op_sel:[0,1] op_sel_hi:[1,0]
	v_mov_b32_e32 v79, v92
	v_mov_b32_e32 v83, v93
	v_mov_b32_e32 v69, v91
	v_mov_b32_e32 v63, v90
	v_pk_add_f32 v[70:71], v[78:79], v[82:83]
	v_pk_add_f32 v[62:63], v[62:63], v[68:69]
	s_nop 0
	v_pk_add_f32 v[62:63], v[62:63], v[70:71]
	s_nop 0
	v_add_f32_e32 v29, v62, v63
	s_nop 1
	v_add_f32_dpp v29, v29, v29 quad_perm:[1,0,3,2] row_mask:0xf bank_mask:0xf bound_ctrl:1
	s_nop 1
	v_add_f32_dpp v29, v29, v29 quad_perm:[2,3,0,1] row_mask:0xf bank_mask:0xf bound_ctrl:1
	s_nop 1
	v_add_f32_dpp v29, v29, v29 row_half_mirror row_mask:0xf bank_mask:0xf bound_ctrl:1
	s_nop 1
	v_add_f32_dpp v29, v29, v29 row_mirror row_mask:0xf bank_mask:0xf bound_ctrl:1
	ds_bpermute_b32 v62, v25, v29
	s_waitcnt lgkmcnt(0)
	v_add_f32_e32 v29, v29, v62
	ds_bpermute_b32 v62, v26, v29
	s_waitcnt lgkmcnt(0)
	v_add_f32_e32 v29, v29, v62
	v_fmamk_f32 v29, v29, 0x3a000000, v27
	v_mul_f32_e32 v62, 0x4f800000, v29
	v_cmp_gt_f32_e32 vcc, s19, v29
	s_nop 1
	v_cndmask_b32_e32 v29, v29, v62, vcc
	v_sqrt_f32_e32 v62, v29
	s_nop 0
	v_add_u32_e32 v63, -1, v62
	v_add_u32_e32 v64, 1, v62
	v_fma_f32 v65, -v63, v62, v29
	v_fma_f32 v66, -v64, v62, v29
	v_cmp_ge_f32_e64 s[0:1], 0, v65
	s_nop 1
	v_cndmask_b32_e64 v62, v62, v63, s[0:1]
	v_cmp_lt_f32_e64 s[0:1], 0, v66
	s_nop 1
	v_cndmask_b32_e64 v62, v62, v64, s[0:1]
	v_mul_f32_e32 v63, 0x37800000, v62
	v_cndmask_b32_e32 v62, v62, v63, vcc
	v_cmp_class_f32_e32 vcc, v29, v28
	s_nop 1
	v_cndmask_b32_e32 v29, v62, v29, vcc
	v_div_scale_f32 v62, s[0:1], v29, v29, 1.0
	v_rcp_f32_e32 v64, v62
	v_div_scale_f32 v63, vcc, 1.0, v29, 1.0
	v_fma_f32 v65, -v62, v64, 1.0
	v_fmac_f32_e32 v64, v65, v64
	v_mul_f32_e32 v65, v63, v64
	v_fma_f32 v66, -v62, v65, v63
	v_fmac_f32_e32 v65, v66, v64
	v_fma_f32 v62, -v62, v65, v63
	v_div_fmas_f32 v62, v62, v64, v65
	v_div_fixup_f32 v62, v62, v29, 1.0
	v_pk_mul_f32 v[42:43], v[42:43], v[62:63] op_sel_hi:[1,0]
	v_pk_mul_f32 v[44:45], v[44:45], v[62:63] op_sel_hi:[1,0]
	v_pk_mul_f32 v[0:1], v[176:177], v[42:43]
	v_pk_mul_f32 v[2:3], v[178:179], v[44:45]
	global_store_dwordx4 v[22:23], v[0:3], off
	v_pk_mul_f32 v[32:33], v[32:33], v[62:63] op_sel_hi:[1,0]
	v_pk_mul_f32 v[30:31], v[30:31], v[62:63] op_sel_hi:[1,0]
	v_pk_mul_f32 v[210:211], v[182:183], v[32:33]
	v_pk_mul_f32 v[208:209], v[180:181], v[30:31]
	global_store_dwordx4 v[22:23], v[208:211], off offset:1024
	v_pk_mul_f32 v[30:31], v[36:37], v[62:63] op_sel_hi:[1,0]
	v_pk_mul_f32 v[32:33], v[34:35], v[62:63] op_sel_hi:[1,0]
	v_pk_mul_f32 v[2:3], v[186:187], v[30:31]
	v_pk_mul_f32 v[0:1], v[184:185], v[32:33]
	global_store_dwordx4 v[22:23], v[0:3], off offset:2048
	v_pk_mul_f32 v[30:31], v[40:41], v[62:63] op_sel_hi:[1,0]
	v_pk_mul_f32 v[32:33], v[38:39], v[62:63] op_sel_hi:[1,0]
	v_pk_mul_f32 v[210:211], v[190:191], v[30:31]
	v_pk_mul_f32 v[208:209], v[188:189], v[32:33]
	global_store_dwordx4 v[22:23], v[208:211], off offset:3072
	v_add_co_u32_e32 v22, vcc, s17, v22
	v_pk_mul_f32 v[30:31], v[48:49], v[62:63] op_sel_hi:[1,0]
	v_pk_mul_f32 v[32:33], v[46:47], v[62:63] op_sel_hi:[1,0]
	v_addc_co_u32_e32 v23, vcc, 0, v23, vcc
	v_pk_mul_f32 v[0:1], v[192:193], v[32:33]
	v_pk_mul_f32 v[2:3], v[194:195], v[30:31]
	global_store_dwordx4 v[22:23], v[0:3], off
	v_pk_mul_f32 v[30:31], v[52:53], v[62:63] op_sel_hi:[1,0]
	v_pk_mul_f32 v[32:33], v[50:51], v[62:63] op_sel_hi:[1,0]
	v_pk_mul_f32 v[210:211], v[198:199], v[30:31]
	v_pk_mul_f32 v[208:209], v[196:197], v[32:33]
	global_store_dwordx4 v[22:23], v[208:211], off offset:1024
	v_pk_mul_f32 v[30:31], v[56:57], v[62:63] op_sel_hi:[1,0]
	v_pk_mul_f32 v[32:33], v[54:55], v[62:63] op_sel_hi:[1,0]
	v_pk_mul_f32 v[2:3], v[202:203], v[30:31]
	v_pk_mul_f32 v[0:1], v[200:201], v[32:33]
	global_store_dwordx4 v[22:23], v[0:3], off offset:2048
	v_pk_mul_f32 v[30:31], v[60:61], v[62:63] op_sel_hi:[1,0]
	v_pk_mul_f32 v[32:33], v[58:59], v[62:63] op_sel_hi:[1,0]
	v_pk_mul_f32 v[210:211], v[206:207], v[30:31]
	v_pk_mul_f32 v[208:209], v[204:205], v[32:33]
	global_store_dwordx4 v[22:23], v[208:211], off offset:3072
	s_cbranch_scc1 .LBB0_2447
	s_endpgm
